# lru gate step: the twelve weight fragments of column tiles 1..3 requested behind tile 0's loads instead of one exposed round trip each
# baseline (speedup 1.0000x reference)
.LBB0_370:
	v_ashrrev_i32_e32 v11, 6, v30
	v_add_u32_e32 v8, v111, v104
	s_waitcnt lgkmcnt(0)
	s_barrier
	v_lshl_add_u32 v22, v11, 8, v8
	ds_read2st64_b32 v[112:113], v22 offset1:1
	ds_read2st64_b32 v[114:115], v22 offset0:2 offset1:3
	ds_read2st64_b32 v[116:117], v22 offset0:8 offset1:9
	ds_read2st64_b32 v[118:119], v22 offset0:10 offset1:11
	ds_read2st64_b32 v[120:121], v22 offset0:16 offset1:17
	ds_read2st64_b32 v[122:123], v22 offset0:18 offset1:19
	ds_read2st64_b32 v[124:125], v22 offset0:24 offset1:25
	ds_read2st64_b32 v[126:127], v22 offset0:26 offset1:27
	ds_read2st64_b32 v[128:129], v22 offset0:32 offset1:33
	ds_read2st64_b32 v[130:131], v22 offset0:34 offset1:35
	ds_read2st64_b32 v[132:133], v22 offset0:40 offset1:41
	ds_read2st64_b32 v[134:135], v22 offset0:42 offset1:43
	ds_read2st64_b32 v[136:137], v22 offset0:48 offset1:49
	ds_read2st64_b32 v[138:139], v22 offset0:50 offset1:51
	ds_read2st64_b32 v[140:141], v22 offset0:56 offset1:57
	ds_read2st64_b32 v[142:143], v22 offset0:58 offset1:59
	v_lshlrev_b32_e32 v9, 1, v31
	s_movk_i32 s0, 0x104
	v_sub_u32_e32 v10, v8, v9
	v_mad_u64_u32 v[8:9], s[0:1], v11, s0, v[8:9]
	s_waitcnt vmcnt(12) lgkmcnt(0)
	v_fma_f32 v23, v15, v112, v14
	v_fmac_f32_e32 v23, v21, v113
	v_mad_u64_u32 v[10:11], s[0:1], v11, s39, v[10:11]
	s_or_b32 s0, s24, s71
	s_ashr_i32 s1, s0, 31
	v_fmac_f32_e32 v23, v12, v114
	v_fmac_f32_e32 v23, v13, v115
	ds_write_b32 v8, v23 offset:17408
	v_bfe_u32 v9, v23, 16, 1
	v_add3_u32 v9, v23, v9, s25
	ds_write_b16_d16_hi v10, v9 offset:34304
	s_lshl_b64 s[0:1], s[0:1], 13
	v_fma_f32 v9, v15, v116, v14
	v_fmac_f32_e32 v9, v21, v117
	s_add_u32 s2, s69, s0
	s_addc_u32 s3, s70, s1
	v_and_b32_e32 v24, 48, v30
	v_mov_b32_e32 v25, v105
	v_fmac_f32_e32 v9, v12, v118
	v_fmac_f32_e32 v9, v13, v119
	ds_write_b32 v8, v9 offset:19488
	v_bfe_u32 v11, v9, 16, 1
	v_add3_u32 v9, v9, v11, s25
	ds_write_b16_d16_hi v10, v9 offset:35456
	s_or_b32 s0, s24, s72
	v_fma_f32 v9, v15, v120, v14
	v_fmac_f32_e32 v9, v21, v121
	s_ashr_i32 s1, s0, 31
	s_lshl_b64 s[0:1], s[0:1], 13
	s_add_u32 s0, s69, s0
	s_addc_u32 s1, s70, s1
	v_fmac_f32_e32 v9, v12, v122
	v_fmac_f32_e32 v9, v13, v123
	ds_write_b32 v8, v9 offset:21568
	v_bfe_u32 v11, v9, 16, 1
	v_add3_u32 v9, v9, v11, s25
	ds_write_b16_d16_hi v10, v9 offset:36608
	s_mov_b32 s14, 0xbfb8aa3b
	v_fma_f32 v9, v15, v124, v14
	v_fmac_f32_e32 v9, v21, v125
	v_or_b32_e32 v47, 16, v35
	v_cmp_gt_u32_e32 vcc, s21, v30
	v_mov_b32_e32 v67, 1.0
	v_mov_b32_e32 v68, 0
	v_fmac_f32_e32 v9, v12, v126
	v_fmac_f32_e32 v9, v13, v127
	ds_write_b32 v8, v9 offset:23648
	v_bfe_u32 v11, v9, 16, 1
	v_add3_u32 v9, v9, v11, s25
	ds_write_b16_d16_hi v10, v9 offset:37760
	v_fma_f32 v9, v15, v128, v14
	v_fmac_f32_e32 v9, v21, v129
	v_fmac_f32_e32 v9, v12, v130
	v_fmac_f32_e32 v9, v13, v131
	ds_write_b32 v8, v9 offset:25728
	v_bfe_u32 v11, v9, 16, 1
	v_add3_u32 v9, v9, v11, s25
	ds_write_b16_d16_hi v10, v9 offset:38912
	v_fma_f32 v9, v15, v132, v14
	v_fmac_f32_e32 v9, v21, v133
	v_fmac_f32_e32 v9, v12, v134
	v_fmac_f32_e32 v9, v13, v135
	ds_write_b32 v8, v9 offset:27808
	v_bfe_u32 v11, v9, 16, 1
	v_add3_u32 v9, v9, v11, s25
	ds_write_b16_d16_hi v10, v9 offset:40064
	v_fma_f32 v9, v15, v136, v14
	v_fmac_f32_e32 v9, v21, v137
	v_fmac_f32_e32 v9, v12, v138
	v_fmac_f32_e32 v9, v13, v139
	ds_write_b32 v8, v9 offset:29888
	v_bfe_u32 v11, v9, 16, 1
	v_add3_u32 v9, v9, v11, s25
	ds_write_b16_d16_hi v10, v9 offset:41216
	v_fmac_f32_e32 v14, v15, v140
	v_fmac_f32_e32 v14, v21, v141
	v_fmac_f32_e32 v14, v12, v142
	v_fmac_f32_e32 v14, v13, v143
	ds_write_b32 v8, v14 offset:31968
	v_bfe_u32 v8, v14, 16, 1
	v_add3_u32 v8, v14, v8, s25
	v_lshrrev_b32_e32 v16, 2, v30
	ds_write_b16_d16_hi v10, v8 offset:42368
	v_or_b32_e32 v8, s34, v35
	v_and_or_b32 v21, v16, 12, s34
	v_lshlrev_b32_e32 v16, 7, v35
	v_mov_b32_e32 v17, v105
	v_mul_u32_u24_e32 v8, 0x90, v8
	v_lshl_add_u64 v[22:23], s[2:3], 0, v[16:17]
	s_waitcnt lgkmcnt(0)
	s_barrier
	v_add3_u32 v8, v111, v8, v24
	v_lshl_add_u64 v[22:23], v[22:23], 0, v[24:25]
	ds_read_b128 v[12:15], v8 offset:34304
	ds_read_b128 v[8:11], v8 offset:34368
	global_load_dwordx4 v[36:39], v[22:23], off
	global_load_dwordx4 v[48:51], v[22:23], off offset:64
	v_lshl_add_u64 v[16:17], s[0:1], 0, v[16:17]
	v_lshl_add_u64 v[16:17], v[16:17], 0, v[24:25]
	v_lshlrev_b32_e32 v42, 6, v21
	s_waitcnt vmcnt(1) lgkmcnt(1)
	v_mfma_f32_16x16x32_bf16 v[36:39], v[12:15], v[36:39], 0
	global_load_dwordx4 v[52:55], v[16:17], off offset:64
	s_waitcnt vmcnt(1) lgkmcnt(0)
	v_mfma_f32_16x16x32_bf16 v[48:51], v[8:11], v[48:51], v[36:39]
	s_nop 4
	global_load_dwordx4 v[36:39], v[16:17], off
	s_mov_b64 s[100:101], 0x1000
	v_lshl_add_u64 v[180:181], v[22:23], 0, s[100:101]
	v_lshl_add_u64 v[72:73], v[16:17], 0, s[100:101]
	global_load_dwordx4 v[216:219], v[22:23], off offset:2048
	global_load_dwordx4 v[220:223], v[22:23], off offset:2112
	global_load_dwordx4 v[224:227], v[16:17], off offset:2048
	global_load_dwordx4 v[228:231], v[16:17], off offset:2112
	global_load_dwordx4 v[232:235], v[180:181], off
	global_load_dwordx4 v[236:239], v[180:181], off offset:64
	global_load_dwordx4 v[240:243], v[72:73], off
	global_load_dwordx4 v[244:247], v[72:73], off offset:64
	global_load_dwordx4 v[248:251], v[180:181], off offset:2048
	global_load_dwordx4 v[200:203], v[180:181], off offset:2112
	global_load_dwordx4 v[204:207], v[72:73], off offset:2048
	global_load_dwordx4 v[208:211], v[72:73], off offset:2112
	v_mul_f32_e64 v17, |v20|, s14
	s_nop 0
	v_add_f32_e32 v22, v18, v48
	v_mul_f32_e32 v22, 0xbfb8aa3b, v22
	v_exp_f32_e32 v17, v17
	v_exp_f32_e32 v22, v22
	v_max_f32_e64 v16, -v20, -v20
	v_max_f32_e32 v16, 0, v16
	v_add_f32_e32 v17, 1.0, v17
	v_add_f32_e32 v22, 1.0, v22
	v_log_f32_e32 v17, v17
	v_rcp_f32_e32 v22, v22
	v_or_b32_e32 v20, s73, v35
	v_lshlrev_b32_e32 v48, 7, v47
	v_fmac_f32_e32 v16, 0x3f317218, v17
	v_mul_f32_e32 v22, 0xc1000000, v22
	v_mul_f32_e32 v22, v16, v22
	v_mul_f32_e32 v22, 0x3fb8aa3b, v22
	v_exp_f32_e32 v22, v22
	v_lshlrev_b32_e32 v17, 2, v35
	s_waitcnt vmcnt(12)
	v_mfma_f32_16x16x32_bf16 v[36:39], v[12:15], v[36:39], 0
	v_mfma_f32_16x16x32_bf16 v[52:55], v[8:11], v[52:55], v[36:39]
	s_nop 6
	v_fma_f32 v36, -v22, v22, 1.0
	v_max_f32_e32 v36, 0, v36
	v_add_f32_e32 v23, v19, v52
	v_mul_f32_e32 v23, 0xbfb8aa3b, v23
	v_exp_f32_e32 v23, v23
	v_sqrt_f32_e32 v36, v36
	v_or_b32_e32 v39, 64, v42
	v_or_b32_e32 v38, 0x80, v42
	v_add_f32_e32 v23, 1.0, v23
	v_rcp_f32_e32 v23, v23
	v_or_b32_e32 v37, 0xc0, v42
	v_mul_f32_e32 v23, v23, v36
	v_mul_u32_u24_e32 v36, 0x104, v21
	v_add3_u32 v36, v111, v17, v36
	ds_read_b32 v144, v36 offset:17408
	ds_read_b32 v145, v36 offset:17668
	ds_read_b32 v146, v36 offset:17928
	ds_read_b32 v147, v36 offset:18188
	ds_read_b32 v148, v36 offset:17472
	ds_read_b32 v149, v36 offset:17732
	ds_read_b32 v150, v36 offset:17992
	ds_read_b32 v151, v36 offset:18252
	ds_read_b32 v152, v36 offset:17536
	ds_read_b32 v153, v36 offset:17796
	ds_read_b32 v154, v36 offset:18056
	ds_read_b32 v155, v36 offset:18316
	ds_read_b32 v156, v36 offset:17600
	ds_read_b32 v157, v36 offset:17860
	ds_read_b32 v158, v36 offset:18120
	ds_read_b32 v159, v36 offset:18380
	v_or_b32_e32 v21, v42, v20
	v_lshlrev_b32_e32 v21, 2, v21
	s_waitcnt lgkmcnt(0)
	v_mul_f32_e32 v17, v144, v23
	v_add_u32_e32 v23, v111, v21
	v_add_u32_e32 v21, v28, v21
	ds_write_b32 v23, v22 offset:43520
	ds_write_b32 v21, v17
	v_add_f32_e32 v17, v18, v49
	v_mul_f32_e32 v17, 0xbfb8aa3b, v17
	v_exp_f32_e32 v17, v17
	v_add_f32_e32 v21, v19, v53
	v_mul_f32_e32 v21, 0xbfb8aa3b, v21
	v_exp_f32_e32 v21, v21
	v_add_f32_e32 v17, 1.0, v17
	v_rcp_f32_e32 v17, v17
	v_mov_b32_e32 v49, v105
	v_add_f32_e32 v21, 1.0, v21
	v_rcp_f32_e32 v21, v21
	v_mul_f32_e32 v17, 0xc1000000, v17
	v_mul_f32_e32 v17, v16, v17
	v_mul_f32_e32 v17, 0x3fb8aa3b, v17
	v_exp_f32_e32 v17, v17
	s_nop 0
	v_fma_f32 v22, -v17, v17, 1.0
	v_max_f32_e32 v22, 0, v22
	v_sqrt_f32_e32 v22, v22
	s_nop 0
	v_mul_f32_e32 v21, v21, v22
	v_mul_f32_e32 v21, v145, v21
	v_or_b32_e32 v22, v39, v20
	v_lshlrev_b32_e32 v22, 2, v22
	v_add_u32_e32 v23, v111, v22
	ds_write_b32 v23, v17 offset:43520
	v_add_u32_e32 v17, v28, v22
	ds_write_b32 v17, v21
	v_add_f32_e32 v17, v18, v50
	v_mul_f32_e32 v17, 0xbfb8aa3b, v17
	v_exp_f32_e32 v17, v17
	v_add_f32_e32 v21, v19, v54
	v_mul_f32_e32 v21, 0xbfb8aa3b, v21
	v_exp_f32_e32 v21, v21
	v_add_f32_e32 v17, 1.0, v17
	v_rcp_f32_e32 v17, v17
	v_add_f32_e32 v21, 1.0, v21
	v_rcp_f32_e32 v21, v21
	v_mul_f32_e32 v17, 0xc1000000, v17
	v_mul_f32_e32 v17, v16, v17
	v_mul_f32_e32 v17, 0x3fb8aa3b, v17
	v_exp_f32_e32 v17, v17
	s_nop 0
	v_fma_f32 v22, -v17, v17, 1.0
	v_max_f32_e32 v22, 0, v22
	v_sqrt_f32_e32 v22, v22
	s_nop 0
	v_mul_f32_e32 v21, v21, v22
	v_mul_f32_e32 v21, v146, v21
	v_or_b32_e32 v22, v38, v20
	v_lshlrev_b32_e32 v22, 2, v22
	v_add_u32_e32 v23, v111, v22
	ds_write_b32 v23, v17 offset:43520
	v_add_u32_e32 v17, v28, v22
	ds_write_b32 v17, v21
	v_add_f32_e32 v17, v18, v51
	v_mul_f32_e32 v17, 0xbfb8aa3b, v17
	v_exp_f32_e32 v17, v17
	v_add_f32_e32 v18, v19, v55
	v_mul_f32_e32 v18, 0xbfb8aa3b, v18
	v_exp_f32_e32 v18, v18
	v_add_f32_e32 v17, 1.0, v17
	v_rcp_f32_e32 v17, v17
	v_add_f32_e32 v18, 1.0, v18
	v_rcp_f32_e32 v18, v18
	v_mul_f32_e32 v17, 0xc1000000, v17
	v_mul_f32_e32 v16, v16, v17
	v_mul_f32_e32 v16, 0x3fb8aa3b, v16
	v_exp_f32_e32 v16, v16
	s_nop 0
	v_fma_f32 v17, -v16, v16, 1.0
	v_max_f32_e32 v17, 0, v17
	v_sqrt_f32_e32 v17, v17
	s_nop 0
	v_mul_f32_e32 v17, v18, v17
	v_mul_f32_e32 v17, v147, v17
	v_or_b32_e32 v18, v37, v20
	v_lshlrev_b32_e32 v18, 2, v18
	v_add_u32_e32 v19, v111, v18
	ds_write_b32 v19, v16 offset:43520
	v_add_u32_e32 v16, v28, v18
	ds_write_b32 v16, v17
	v_lshl_add_u64 v[16:17], s[2:3], 0, v[48:49]
	v_lshl_add_u64 v[20:21], v[16:17], 0, v[24:25]
	s_waitcnt vmcnt(0)
	v_mfma_f32_16x16x32_bf16 v[16:19], v[12:15], v[216:219], 0
	s_waitcnt vmcnt(0)
	v_mfma_f32_16x16x32_bf16 v[16:19], v[8:11], v[220:223], v[16:19]
	v_lshl_add_u64 v[20:21], s[0:1], 0, v[48:49]
	v_lshl_add_u64 v[48:49], v[20:21], 0, v[24:25]
	s_waitcnt vmcnt(0)
	v_mfma_f32_16x16x32_bf16 v[20:23], v[12:15], v[224:227], 0
	s_nop 1
	v_add_f32_e32 v16, v45, v16
	v_mul_f32_e32 v16, 0xbfb8aa3b, v16
	s_waitcnt vmcnt(0)
	v_mfma_f32_16x16x32_bf16 v[20:23], v[8:11], v[228:231], v[20:23]
	v_max_f32_e64 v48, -v46, -v46
	v_mul_f32_e64 v46, |v46|, s14
	v_exp_f32_e32 v46, v46
	v_exp_f32_e32 v16, v16
	v_max_f32_e32 v49, 0, v48
	s_nop 2
	v_add_f32_e32 v20, v44, v20
	v_add_f32_e32 v46, 1.0, v46
	v_add_f32_e32 v16, 1.0, v16
	v_log_f32_e32 v46, v46
	v_rcp_f32_e32 v16, v16
	v_mul_f32_e32 v20, 0xbfb8aa3b, v20
	v_exp_f32_e32 v20, v20
	v_fmac_f32_e32 v49, 0x3f317218, v46
	v_mul_f32_e32 v16, 0xc1000000, v16
	v_mul_f32_e32 v16, v49, v16
	v_mul_f32_e32 v16, 0x3fb8aa3b, v16
	v_exp_f32_e32 v16, v16
	v_add_f32_e32 v20, 1.0, v20
	v_rcp_f32_e32 v20, v20
	v_add_u32_e32 v51, s73, v35
	v_fma_f32 v46, -v16, v16, 1.0
	v_max_f32_e32 v46, 0, v46
	v_sqrt_f32_e32 v46, v46
	v_or_b32_e32 v50, s73, v47
	v_add_u32_e32 v47, v42, v51
	v_lshl_add_u32 v48, v47, 2, v111
	v_mul_f32_e32 v20, v20, v46
	ds_write_b32 v48, v16 offset:43584
	v_mul_f32_e32 v20, v148, v20
	v_or_b32_e32 v46, v42, v50
	v_lshl_add_u32 v16, v46, 2, v28
	ds_write_b32 v16, v20
	v_add_f32_e32 v16, v45, v17
	v_mul_f32_e32 v16, 0xbfb8aa3b, v16
	v_exp_f32_e32 v16, v16
	v_add_f32_e32 v17, v44, v21
	v_mul_f32_e32 v17, 0xbfb8aa3b, v17
	v_exp_f32_e32 v17, v17
	v_add_f32_e32 v16, 1.0, v16
	v_rcp_f32_e32 v16, v16
	v_add_u32_e32 v21, v39, v51
	v_add_f32_e32 v17, 1.0, v17
	v_rcp_f32_e32 v17, v17
	v_mul_f32_e32 v16, 0xc1000000, v16
	v_mul_f32_e32 v16, v49, v16
	v_mul_f32_e32 v16, 0x3fb8aa3b, v16
	v_exp_f32_e32 v16, v16
	v_lshl_add_u32 v47, v21, 2, v111
	v_fma_f32 v20, -v16, v16, 1.0
	v_max_f32_e32 v20, 0, v20
	v_sqrt_f32_e32 v20, v20
	s_nop 0
	v_mul_f32_e32 v17, v17, v20
	ds_write_b32 v47, v16 offset:43584
	v_mul_f32_e32 v17, v149, v17
	v_or_b32_e32 v20, v39, v50
	v_lshl_add_u32 v16, v20, 2, v28
	ds_write_b32 v16, v17
	v_add_f32_e32 v16, v45, v18
	v_mul_f32_e32 v16, 0xbfb8aa3b, v16
	v_exp_f32_e32 v16, v16
	v_add_f32_e32 v17, v44, v22
	v_mul_f32_e32 v17, 0xbfb8aa3b, v17
	v_exp_f32_e32 v17, v17
	v_add_f32_e32 v16, 1.0, v16
	v_rcp_f32_e32 v16, v16
	v_add_u32_e32 v20, v38, v51
	v_add_f32_e32 v17, 1.0, v17
	v_rcp_f32_e32 v17, v17
	v_mul_f32_e32 v16, 0xc1000000, v16
	v_mul_f32_e32 v16, v49, v16
	v_mul_f32_e32 v16, 0x3fb8aa3b, v16
	v_exp_f32_e32 v16, v16
	v_lshl_add_u32 v46, v20, 2, v111
	v_fma_f32 v18, -v16, v16, 1.0
	v_max_f32_e32 v18, 0, v18
	v_sqrt_f32_e32 v18, v18
	s_nop 0
	v_mul_f32_e32 v17, v17, v18
	ds_write_b32 v46, v16 offset:43584
	v_mul_f32_e32 v17, v150, v17
	v_or_b32_e32 v18, v38, v50
	v_lshl_add_u32 v16, v18, 2, v28
	ds_write_b32 v16, v17
	v_add_f32_e32 v16, v45, v19
	v_mul_f32_e32 v16, 0xbfb8aa3b, v16
	v_exp_f32_e32 v16, v16
	v_add_f32_e32 v17, v44, v23
	v_mul_f32_e32 v17, 0xbfb8aa3b, v17
	v_exp_f32_e32 v17, v17
	v_add_f32_e32 v16, 1.0, v16
	v_rcp_f32_e32 v16, v16
	v_add_u32_e32 v19, v37, v51
	v_add_f32_e32 v17, 1.0, v17
	v_rcp_f32_e32 v17, v17
	v_mul_f32_e32 v16, 0xc1000000, v16
	v_mul_f32_e32 v16, v49, v16
	v_mul_f32_e32 v16, 0x3fb8aa3b, v16
	v_exp_f32_e32 v16, v16
	v_lshl_add_u32 v44, v19, 2, v111
	v_or_b32_e32 v45, 32, v35
	v_mov_b32_e32 v51, v105
	v_fma_f32 v18, -v16, v16, 1.0
	v_max_f32_e32 v18, 0, v18
	v_sqrt_f32_e32 v18, v18
	v_max_f32_e64 v49, -v43, -v43
	v_mul_f32_e64 v43, |v43|, s14
	v_exp_f32_e32 v43, v43
	v_mul_f32_e32 v17, v17, v18
	ds_write_b32 v44, v16 offset:43584
	v_add_f32_e32 v43, 1.0, v43
	v_log_f32_e32 v43, v43
	v_max_f32_e32 v49, 0, v49
	v_mul_f32_e32 v17, v151, v17
	v_or_b32_e32 v18, v37, v50
	v_lshl_add_u32 v16, v18, 2, v28
	v_lshlrev_b32_e32 v50, 7, v45
	ds_write_b32 v16, v17
	v_lshl_add_u64 v[16:17], s[2:3], 0, v[50:51]
	v_lshl_add_u64 v[20:21], v[16:17], 0, v[24:25]
	s_waitcnt vmcnt(0)
	v_mfma_f32_16x16x32_bf16 v[16:19], v[12:15], v[232:235], 0
	v_fmac_f32_e32 v49, 0x3f317218, v43
	v_or_b32_e32 v43, s73, v45
	s_waitcnt vmcnt(0)
	v_mfma_f32_16x16x32_bf16 v[16:19], v[8:11], v[236:239], v[16:19]
	v_lshl_add_u64 v[20:21], s[0:1], 0, v[50:51]
	v_lshl_add_u64 v[50:51], v[20:21], 0, v[24:25]
	s_nop 4
	v_add_f32_e32 v16, v41, v16
	v_mul_f32_e32 v16, 0xbfb8aa3b, v16
	v_exp_f32_e32 v16, v16
	s_waitcnt vmcnt(1)
	v_mfma_f32_16x16x32_bf16 v[20:23], v[12:15], v[240:243], 0
	v_add_f32_e32 v16, 1.0, v16
	v_rcp_f32_e32 v16, v16
	v_or_b32_e32 v35, 48, v35
	s_waitcnt vmcnt(0)
	v_mfma_f32_16x16x32_bf16 v[20:23], v[8:11], v[244:247], v[20:23]
	v_mul_f32_e32 v16, 0xc1000000, v16
	v_mul_f32_e32 v16, v49, v16
	v_mul_f32_e32 v16, 0x3fb8aa3b, v16
	v_exp_f32_e32 v16, v16
	s_nop 3
	v_add_f32_e32 v20, v40, v20
	v_mul_f32_e32 v20, 0xbfb8aa3b, v20
	v_exp_f32_e32 v20, v20
	v_fma_f32 v45, -v16, v16, 1.0
	v_max_f32_e32 v45, 0, v45
	v_sqrt_f32_e32 v45, v45
	v_add_f32_e32 v20, 1.0, v20
	v_rcp_f32_e32 v20, v20
	s_nop 0
	v_mul_f32_e32 v20, v20, v45
	ds_write_b32 v48, v16 offset:43648
	v_mul_f32_e32 v20, v152, v20
	v_or_b32_e32 v45, v42, v43
	v_lshl_add_u32 v16, v45, 2, v28
	ds_write_b32 v16, v20
	v_add_f32_e32 v16, v41, v17
	v_mul_f32_e32 v16, 0xbfb8aa3b, v16
	v_exp_f32_e32 v16, v16
	v_add_f32_e32 v17, v40, v21
	v_mul_f32_e32 v17, 0xbfb8aa3b, v17
	v_exp_f32_e32 v17, v17
	v_add_f32_e32 v16, 1.0, v16
	v_rcp_f32_e32 v16, v16
	v_add_f32_e32 v17, 1.0, v17
	v_rcp_f32_e32 v17, v17
	v_mul_f32_e32 v16, 0xc1000000, v16
	v_mul_f32_e32 v16, v49, v16
	v_mul_f32_e32 v16, 0x3fb8aa3b, v16
	v_exp_f32_e32 v16, v16
	s_nop 0
	v_fma_f32 v20, -v16, v16, 1.0
	v_max_f32_e32 v20, 0, v20
	v_sqrt_f32_e32 v20, v20
	s_nop 0
	v_mul_f32_e32 v17, v17, v20
	ds_write_b32 v47, v16 offset:43648
	v_mul_f32_e32 v17, v153, v17
	v_or_b32_e32 v20, v39, v43
	v_lshl_add_u32 v16, v20, 2, v28
	ds_write_b32 v16, v17
	v_add_f32_e32 v16, v41, v18
	v_mul_f32_e32 v16, 0xbfb8aa3b, v16
	v_exp_f32_e32 v16, v16
	v_add_f32_e32 v17, v40, v22
	v_mul_f32_e32 v17, 0xbfb8aa3b, v17
	v_exp_f32_e32 v17, v17
	v_add_f32_e32 v16, 1.0, v16
	v_rcp_f32_e32 v16, v16
	v_add_f32_e32 v17, 1.0, v17
	v_rcp_f32_e32 v17, v17
	v_mul_f32_e32 v16, 0xc1000000, v16
	v_mul_f32_e32 v16, v49, v16
	v_mul_f32_e32 v16, 0x3fb8aa3b, v16
	v_exp_f32_e32 v16, v16
	s_nop 0
	v_fma_f32 v18, -v16, v16, 1.0
	v_max_f32_e32 v18, 0, v18
	v_sqrt_f32_e32 v18, v18
	s_nop 0
	v_mul_f32_e32 v17, v17, v18
	ds_write_b32 v46, v16 offset:43648
	v_mul_f32_e32 v17, v154, v17
	v_or_b32_e32 v18, v38, v43
	v_lshl_add_u32 v16, v18, 2, v28
	ds_write_b32 v16, v17
	v_add_f32_e32 v16, v41, v19
	v_mul_f32_e32 v16, 0xbfb8aa3b, v16
	v_exp_f32_e32 v16, v16
	v_add_f32_e32 v17, v40, v23
	v_mul_f32_e32 v17, 0xbfb8aa3b, v17
	v_exp_f32_e32 v17, v17
	v_add_f32_e32 v16, 1.0, v16
	v_rcp_f32_e32 v16, v16
	v_lshlrev_b32_e32 v40, 7, v35
	v_add_f32_e32 v17, 1.0, v17
	v_rcp_f32_e32 v17, v17
	v_mul_f32_e32 v16, 0xc1000000, v16
	v_mul_f32_e32 v16, v49, v16
	v_mul_f32_e32 v16, 0x3fb8aa3b, v16
	v_exp_f32_e32 v16, v16
	v_mov_b32_e32 v41, v105
	v_fma_f32 v18, -v16, v16, 1.0
	v_max_f32_e32 v18, 0, v18
	v_sqrt_f32_e32 v18, v18
	s_nop 0
	v_mul_f32_e32 v17, v17, v18
	ds_write_b32 v44, v16 offset:43648
	v_mul_f32_e32 v17, v155, v17
	v_or_b32_e32 v18, v37, v43
	v_lshl_add_u32 v16, v18, 2, v28
	ds_write_b32 v16, v17
	v_lshl_add_u64 v[16:17], s[2:3], 0, v[40:41]
	v_lshl_add_u64 v[20:21], v[16:17], 0, v[24:25]
	s_waitcnt vmcnt(0)
	v_mfma_f32_16x16x32_bf16 v[16:19], v[12:15], v[248:251], 0
	s_waitcnt vmcnt(0)
	v_mfma_f32_16x16x32_bf16 v[16:19], v[8:11], v[200:203], v[16:19]
	v_lshl_add_u64 v[20:21], s[0:1], 0, v[40:41]
	v_lshl_add_u64 v[24:25], v[20:21], 0, v[24:25]
	s_waitcnt vmcnt(0)
	v_mfma_f32_16x16x32_bf16 v[12:15], v[12:15], v[204:207], 0
	s_waitcnt vmcnt(0)
	v_mfma_f32_16x16x32_bf16 v[8:11], v[8:11], v[208:211], v[12:15]
	s_nop 4
	v_add_f32_e32 v14, v33, v16
	v_mul_f32_e64 v13, |v34|, s14
	v_mul_f32_e32 v14, 0xbfb8aa3b, v14
	v_exp_f32_e32 v13, v13
	v_exp_f32_e32 v14, v14
	v_max_f32_e64 v12, -v34, -v34
	v_max_f32_e32 v12, 0, v12
	v_add_f32_e32 v13, 1.0, v13
	v_add_f32_e32 v14, 1.0, v14
	v_log_f32_e32 v13, v13
	v_rcp_f32_e32 v14, v14
	v_add_f32_e32 v8, v32, v8
	v_mul_f32_e32 v8, 0xbfb8aa3b, v8
	v_fmac_f32_e32 v12, 0x3f317218, v13
	v_mul_f32_e32 v14, 0xc1000000, v14
	v_mul_f32_e32 v14, v12, v14
	v_mul_f32_e32 v14, 0x3fb8aa3b, v14
	v_exp_f32_e32 v14, v14
	v_exp_f32_e32 v8, v8
	v_or_b32_e32 v13, s73, v35
	v_add_f32_e32 v9, v32, v9
	v_fma_f32 v15, -v14, v14, 1.0
	v_add_f32_e32 v8, 1.0, v8
	v_max_f32_e32 v15, 0, v15
	v_rcp_f32_e32 v8, v8
	v_sqrt_f32_e32 v15, v15
	v_mul_f32_e32 v9, 0xbfb8aa3b, v9
	v_exp_f32_e32 v9, v9
	v_mul_f32_e32 v8, v8, v15
	ds_write_b32 v48, v14 offset:43712
	v_add_f32_e32 v9, 1.0, v9
	v_rcp_f32_e32 v9, v9
	v_mul_f32_e32 v8, v156, v8
	v_or_b32_e32 v15, v42, v13
	v_lshl_add_u32 v14, v15, 2, v28
	ds_write_b32 v14, v8
	v_add_f32_e32 v8, v33, v17
	v_mul_f32_e32 v8, 0xbfb8aa3b, v8
	v_exp_f32_e32 v8, v8
	s_nop 0
	v_add_f32_e32 v8, 1.0, v8
	v_rcp_f32_e32 v8, v8
	s_nop 0
	v_mul_f32_e32 v8, 0xc1000000, v8
	v_mul_f32_e32 v8, v12, v8
	v_mul_f32_e32 v8, 0x3fb8aa3b, v8
	v_exp_f32_e32 v8, v8
	s_nop 0
	v_fma_f32 v14, -v8, v8, 1.0
	v_max_f32_e32 v14, 0, v14
	v_sqrt_f32_e32 v14, v14
	s_nop 0
	v_mul_f32_e32 v9, v9, v14
	ds_write_b32 v47, v8 offset:43712
	v_mul_f32_e32 v9, v157, v9
	v_or_b32_e32 v14, v39, v13
	v_lshl_add_u32 v8, v14, 2, v28
	ds_write_b32 v8, v9
	v_add_f32_e32 v8, v33, v18
	v_mul_f32_e32 v8, 0xbfb8aa3b, v8
	v_exp_f32_e32 v8, v8
	v_add_f32_e32 v9, v32, v10
	v_mul_f32_e32 v9, 0xbfb8aa3b, v9
	v_exp_f32_e32 v9, v9
	v_add_f32_e32 v8, 1.0, v8
	v_rcp_f32_e32 v8, v8
	v_add_f32_e32 v9, 1.0, v9
	v_rcp_f32_e32 v9, v9
	v_mul_f32_e32 v8, 0xc1000000, v8
	v_mul_f32_e32 v8, v12, v8
	v_mul_f32_e32 v8, 0x3fb8aa3b, v8
	v_exp_f32_e32 v8, v8
	s_nop 0
	v_fma_f32 v10, -v8, v8, 1.0
	v_max_f32_e32 v10, 0, v10
	v_sqrt_f32_e32 v10, v10
	s_nop 0
	v_mul_f32_e32 v9, v9, v10
	ds_write_b32 v46, v8 offset:43712
	v_mul_f32_e32 v9, v158, v9
	v_or_b32_e32 v10, v38, v13
	v_lshl_add_u32 v8, v10, 2, v28
	ds_write_b32 v8, v9
	v_add_f32_e32 v8, v33, v19
	v_mul_f32_e32 v8, 0xbfb8aa3b, v8
	v_exp_f32_e32 v8, v8
	v_add_f32_e32 v9, v32, v11
	v_mul_f32_e32 v9, 0xbfb8aa3b, v9
	v_exp_f32_e32 v9, v9
	v_add_f32_e32 v8, 1.0, v8
	v_rcp_f32_e32 v8, v8
	v_add_f32_e32 v9, 1.0, v9
	v_rcp_f32_e32 v9, v9
	v_mul_f32_e32 v8, 0xc1000000, v8
	v_mul_f32_e32 v8, v12, v8
	v_mul_f32_e32 v8, 0x3fb8aa3b, v8
	v_exp_f32_e32 v8, v8
	v_ashrrev_i32_e32 v12, 8, v30
	v_fma_f32 v10, -v8, v8, 1.0
	v_max_f32_e32 v10, 0, v10
	v_sqrt_f32_e32 v10, v10
	s_nop 0
	v_mul_f32_e32 v9, v9, v10
	ds_write_b32 v44, v8 offset:43712
	v_mul_f32_e32 v9, v159, v9
	v_or_b32_e32 v10, v37, v13
	v_lshl_add_u32 v8, v10, 2, v28
	ds_write_b32 v8, v9
	v_bfe_u32 v8, v30, 6, 2
	v_lshlrev_b32_e32 v9, 4, v8
	v_xor_b32_e32 v10, 63, v9
	v_cndmask_b32_e32 v25, v10, v9, vcc
	v_lshl_or_b32 v10, v12, 14, v104
	v_lshl_or_b32 v11, v25, 8, v10
	s_waitcnt lgkmcnt(0)
	s_barrier
	v_add_u32_e32 v13, v111, v11
	v_add_u32_e32 v11, v28, v11
	s_cbranch_vccz .Lscan_bwd
	ds_read_b32 v22, v11
	ds_read_b32 v17, v13 offset:43520
	ds_read_b32 v15, v11 offset:256
	ds_read_b32 v161, v13 offset:43776
	ds_read_b32 v16, v11 offset:512
	ds_read_b32 v162, v13 offset:44032
	ds_read_b32 v18, v11 offset:768
	ds_read_b32 v163, v13 offset:44288
	ds_read_b32 v33, v11 offset:1024
	ds_read_b32 v164, v13 offset:44544
	ds_read_b32 v34, v11 offset:1280
	ds_read_b32 v165, v13 offset:44800
	ds_read_b32 v35, v11 offset:1536
	ds_read_b32 v166, v13 offset:45056
	ds_read_b32 v42, v11 offset:1792
	ds_read_b32 v167, v13 offset:45312
	ds_read_b32 v43, v11 offset:2048
	ds_read_b32 v168, v13 offset:45568
	ds_read_b32 v44, v11 offset:2304
	ds_read_b32 v169, v13 offset:45824
	ds_read_b32 v51, v11 offset:2560
	ds_read_b32 v170, v13 offset:46080
	ds_read_b32 v52, v11 offset:2816
	ds_read_b32 v171, v13 offset:46336
	ds_read_b32 v53, v11 offset:3072
	ds_read_b32 v172, v13 offset:46592
	ds_read_b32 v60, v11 offset:3328
	ds_read_b32 v173, v13 offset:46848
	ds_read_b32 v61, v11 offset:3584
	ds_read_b32 v174, v13 offset:47104
	ds_read_b32 v32, v11 offset:3840
	ds_read_b32 v175, v13 offset:47360
	s_branch .Lscan_rd
